# v27 plus: first half-step's probability row-sum accumulated behind its P.V MFMAs instead of at the head of the second half-step
# baseline (speedup 1.0000x reference)
.LattA_join:
	v_add_f32_e32 v154, v78, v66
	v_add_f32_e32 v154, v67, v154
	v_add_f32_e32 v154, v79, v154
	v_add_f32_e32 v154, v68, v154
	v_add_f32_e32 v154, v80, v154
	v_add_f32_e32 v154, v69, v154
	v_add_f32_e32 v154, v81, v154
	v_add_f32_e32 v154, v70, v154
	v_add_f32_e32 v154, v71, v154
	v_add_f32_e32 v154, v72, v154
	v_add_f32_e32 v154, v73, v154
	v_add_f32_e32 v154, v74, v154
	v_add_f32_e32 v154, v75, v154
	v_add_f32_e32 v154, v76, v154
	v_add_f32_e32 v154, v77, v154
	s_mov_b64 s[12:13], -1
	s_and_b64 vcc, exec, s[0:1]
	s_cbranch_vccz .LBB0_1242
	s_waitcnt vmcnt(0)
	s_mov_b64 s[12:13], 0

.LBB0_1248:
	v_add_f32_e32 v164, v186, v154
	v_mov_b32_e32 v66, v152
	v_add_f32_e32 v67, 0x41000000, v183
	v_cmp_gt_f32_e32 vcc, v66, v67
	s_cbranch_vccz .LBB0_1235
	v_max_f32_e32 v66, v66, v66
	v_max_f32_e32 v67, v183, v183
	v_max_f32_e32 v67, v67, v66
	v_sub_f32_e32 v66, v183, v67
	v_exp_f32_e32 v66, v66
	v_mov_b32_e32 v183, v67
	v_pk_mul_f32 v[64:65], v[64:65], v[66:67] op_sel_hi:[1,0]
	v_pk_mul_f32 v[62:63], v[62:63], v[66:67] op_sel_hi:[1,0]
	v_pk_mul_f32 v[60:61], v[60:61], v[66:67] op_sel_hi:[1,0]
	v_pk_mul_f32 v[58:59], v[58:59], v[66:67] op_sel_hi:[1,0]
	v_pk_mul_f32 v[56:57], v[56:57], v[66:67] op_sel_hi:[1,0]
	v_pk_mul_f32 v[54:55], v[54:55], v[66:67] op_sel_hi:[1,0]
	v_pk_mul_f32 v[52:53], v[52:53], v[66:67] op_sel_hi:[1,0]
	v_pk_mul_f32 v[50:51], v[50:51], v[66:67] op_sel_hi:[1,0]
	v_pk_mul_f32 v[48:49], v[48:49], v[66:67] op_sel_hi:[1,0]
	v_pk_mul_f32 v[46:47], v[46:47], v[66:67] op_sel_hi:[1,0]
	v_pk_mul_f32 v[44:45], v[44:45], v[66:67] op_sel_hi:[1,0]
	v_pk_mul_f32 v[42:43], v[42:43], v[66:67] op_sel_hi:[1,0]
	v_pk_mul_f32 v[40:41], v[40:41], v[66:67] op_sel_hi:[1,0]
	v_pk_mul_f32 v[38:39], v[38:39], v[66:67] op_sel_hi:[1,0]
	v_pk_mul_f32 v[36:37], v[36:37], v[66:67] op_sel_hi:[1,0]
	v_pk_mul_f32 v[34:35], v[34:35], v[66:67] op_sel_hi:[1,0]
	v_pk_mul_f32 v[32:33], v[32:33], v[66:67] op_sel_hi:[1,0]
	v_pk_mul_f32 v[30:31], v[30:31], v[66:67] op_sel_hi:[1,0]
	v_pk_mul_f32 v[28:29], v[28:29], v[66:67] op_sel_hi:[1,0]
	v_pk_mul_f32 v[26:27], v[26:27], v[66:67] op_sel_hi:[1,0]
	v_pk_mul_f32 v[24:25], v[24:25], v[66:67] op_sel_hi:[1,0]
	v_pk_mul_f32 v[22:23], v[22:23], v[66:67] op_sel_hi:[1,0]
	v_pk_mul_f32 v[20:21], v[20:21], v[66:67] op_sel_hi:[1,0]
	v_pk_mul_f32 v[18:19], v[18:19], v[66:67] op_sel_hi:[1,0]
	v_pk_mul_f32 v[16:17], v[16:17], v[66:67] op_sel_hi:[1,0]
	v_pk_mul_f32 v[14:15], v[14:15], v[66:67] op_sel_hi:[1,0]
	v_pk_mul_f32 v[12:13], v[12:13], v[66:67] op_sel_hi:[1,0]
	v_pk_mul_f32 v[10:11], v[10:11], v[66:67] op_sel_hi:[1,0]
	v_pk_mul_f32 v[8:9], v[8:9], v[66:67] op_sel_hi:[1,0]
	v_pk_mul_f32 v[6:7], v[6:7], v[66:67] op_sel_hi:[1,0]
	v_pk_mul_f32 v[4:5], v[4:5], v[66:67] op_sel_hi:[1,0]
	v_pk_mul_f32 v[2:3], v[2:3], v[66:67] op_sel_hi:[1,0]
	v_mul_f32_e32 v164, v164, v66
	s_branch .LBB0_1235
